# v58 + P4 C-state scan with all 64 chunk loads issued first (hand-written recurrence over registers)
# speedup vs baseline: 1.0078x; 1.0078x over previous
.LBB0_694:
	v_ashrrev_i32_e32 v0, 14, v19
	v_lshlrev_b32_e32 v4, 1, v18
	v_lshlrev_b32_e32 v2, 22, v0
	v_and_or_b32 v2, v4, s10, v2
	v_lshl_add_u32 v20, v0, 8, 0
	v_mov_b32_e32 v14, 0
	v_mov_b32_e32 v15, 0
	s_add_u32 s18, s92, 0x3661c00
	s_addc_u32 s19, s93, 0
	s_add_u32 s20, s92, 0x36ee1c00
	s_addc_u32 s21, s93, 0
	ds_read_b128 v[128:131], v20 offset:0
	ds_read_b128 v[132:135], v20 offset:16
	ds_read_b128 v[136:139], v20 offset:2048
	ds_read_b128 v[140:143], v20 offset:2064
	global_load_dword v64, v2, s[18:19]
	s_add_u32 s18, s18, 0x10000
	s_addc_u32 s19, s19, 0
	global_load_dword v65, v2, s[18:19]
	s_add_u32 s18, s18, 0x10000
	s_addc_u32 s19, s19, 0
	global_load_dword v66, v2, s[18:19]
	s_add_u32 s18, s18, 0x10000
	s_addc_u32 s19, s19, 0
	global_load_dword v67, v2, s[18:19]
	s_add_u32 s18, s18, 0x10000
	s_addc_u32 s19, s19, 0
	global_load_dword v68, v2, s[18:19]
	s_add_u32 s18, s18, 0x10000
	s_addc_u32 s19, s19, 0
	global_load_dword v69, v2, s[18:19]
	s_add_u32 s18, s18, 0x10000
	s_addc_u32 s19, s19, 0
	global_load_dword v70, v2, s[18:19]
	s_add_u32 s18, s18, 0x10000
	s_addc_u32 s19, s19, 0
	global_load_dword v71, v2, s[18:19]
	s_add_u32 s18, s18, 0x10000
	s_addc_u32 s19, s19, 0
	global_load_dword v72, v2, s[18:19]
	s_add_u32 s18, s18, 0x10000
	s_addc_u32 s19, s19, 0
	global_load_dword v73, v2, s[18:19]
	s_add_u32 s18, s18, 0x10000
	s_addc_u32 s19, s19, 0
	global_load_dword v74, v2, s[18:19]
	s_add_u32 s18, s18, 0x10000
	s_addc_u32 s19, s19, 0
	global_load_dword v75, v2, s[18:19]
	s_add_u32 s18, s18, 0x10000
	s_addc_u32 s19, s19, 0
	global_load_dword v76, v2, s[18:19]
	s_add_u32 s18, s18, 0x10000
	s_addc_u32 s19, s19, 0
	global_load_dword v77, v2, s[18:19]
	s_add_u32 s18, s18, 0x10000
	s_addc_u32 s19, s19, 0
	global_load_dword v78, v2, s[18:19]
	s_add_u32 s18, s18, 0x10000
	s_addc_u32 s19, s19, 0
	global_load_dword v79, v2, s[18:19]
	s_add_u32 s18, s18, 0x10000
	s_addc_u32 s19, s19, 0
	global_load_dword v80, v2, s[18:19]
	s_add_u32 s18, s18, 0x10000
	s_addc_u32 s19, s19, 0
	global_load_dword v81, v2, s[18:19]
	s_add_u32 s18, s18, 0x10000
	s_addc_u32 s19, s19, 0
	global_load_dword v82, v2, s[18:19]
	s_add_u32 s18, s18, 0x10000
	s_addc_u32 s19, s19, 0
	global_load_dword v83, v2, s[18:19]
	s_add_u32 s18, s18, 0x10000
	s_addc_u32 s19, s19, 0
	global_load_dword v84, v2, s[18:19]
	s_add_u32 s18, s18, 0x10000
	s_addc_u32 s19, s19, 0
	global_load_dword v85, v2, s[18:19]
	s_add_u32 s18, s18, 0x10000
	s_addc_u32 s19, s19, 0
	global_load_dword v86, v2, s[18:19]
	s_add_u32 s18, s18, 0x10000
	s_addc_u32 s19, s19, 0
	global_load_dword v87, v2, s[18:19]
	s_add_u32 s18, s18, 0x10000
	s_addc_u32 s19, s19, 0
	global_load_dword v88, v2, s[18:19]
	s_add_u32 s18, s18, 0x10000
	s_addc_u32 s19, s19, 0
	global_load_dword v89, v2, s[18:19]
	s_add_u32 s18, s18, 0x10000
	s_addc_u32 s19, s19, 0
	global_load_dword v90, v2, s[18:19]
	s_add_u32 s18, s18, 0x10000
	s_addc_u32 s19, s19, 0
	global_load_dword v91, v2, s[18:19]
	s_add_u32 s18, s18, 0x10000
	s_addc_u32 s19, s19, 0
	global_load_dword v92, v2, s[18:19]
	s_add_u32 s18, s18, 0x10000
	s_addc_u32 s19, s19, 0
	global_load_dword v93, v2, s[18:19]
	s_add_u32 s18, s18, 0x10000
	s_addc_u32 s19, s19, 0
	global_load_dword v94, v2, s[18:19]
	s_add_u32 s18, s18, 0x10000
	s_addc_u32 s19, s19, 0
	global_load_dword v95, v2, s[18:19]
	s_add_u32 s18, s18, 0x10000
	s_addc_u32 s19, s19, 0
	global_load_dword v96, v2, s[18:19]
	s_add_u32 s18, s18, 0x10000
	s_addc_u32 s19, s19, 0
	global_load_dword v97, v2, s[18:19]
	s_add_u32 s18, s18, 0x10000
	s_addc_u32 s19, s19, 0
	global_load_dword v98, v2, s[18:19]
	s_add_u32 s18, s18, 0x10000
	s_addc_u32 s19, s19, 0
	global_load_dword v99, v2, s[18:19]
	s_add_u32 s18, s18, 0x10000
	s_addc_u32 s19, s19, 0
	global_load_dword v100, v2, s[18:19]
	s_add_u32 s18, s18, 0x10000
	s_addc_u32 s19, s19, 0
	global_load_dword v101, v2, s[18:19]
	s_add_u32 s18, s18, 0x10000
	s_addc_u32 s19, s19, 0
	global_load_dword v102, v2, s[18:19]
	s_add_u32 s18, s18, 0x10000
	s_addc_u32 s19, s19, 0
	global_load_dword v103, v2, s[18:19]
	s_add_u32 s18, s18, 0x10000
	s_addc_u32 s19, s19, 0
	global_load_dword v104, v2, s[18:19]
	s_add_u32 s18, s18, 0x10000
	s_addc_u32 s19, s19, 0
	global_load_dword v105, v2, s[18:19]
	s_add_u32 s18, s18, 0x10000
	s_addc_u32 s19, s19, 0
	global_load_dword v106, v2, s[18:19]
	s_add_u32 s18, s18, 0x10000
	s_addc_u32 s19, s19, 0
	global_load_dword v107, v2, s[18:19]
	s_add_u32 s18, s18, 0x10000
	s_addc_u32 s19, s19, 0
	global_load_dword v108, v2, s[18:19]
	s_add_u32 s18, s18, 0x10000
	s_addc_u32 s19, s19, 0
	global_load_dword v109, v2, s[18:19]
	s_add_u32 s18, s18, 0x10000
	s_addc_u32 s19, s19, 0
	global_load_dword v110, v2, s[18:19]
	s_add_u32 s18, s18, 0x10000
	s_addc_u32 s19, s19, 0
	global_load_dword v111, v2, s[18:19]
	s_add_u32 s18, s18, 0x10000
	s_addc_u32 s19, s19, 0
	global_load_dword v112, v2, s[18:19]
	s_add_u32 s18, s18, 0x10000
	s_addc_u32 s19, s19, 0
	global_load_dword v113, v2, s[18:19]
	s_add_u32 s18, s18, 0x10000
	s_addc_u32 s19, s19, 0
	global_load_dword v114, v2, s[18:19]
	s_add_u32 s18, s18, 0x10000
	s_addc_u32 s19, s19, 0
	global_load_dword v115, v2, s[18:19]
	s_add_u32 s18, s18, 0x10000
	s_addc_u32 s19, s19, 0
	global_load_dword v116, v2, s[18:19]
	s_add_u32 s18, s18, 0x10000
	s_addc_u32 s19, s19, 0
	global_load_dword v117, v2, s[18:19]
	s_add_u32 s18, s18, 0x10000
	s_addc_u32 s19, s19, 0
	global_load_dword v118, v2, s[18:19]
	s_add_u32 s18, s18, 0x10000
	s_addc_u32 s19, s19, 0
	global_load_dword v119, v2, s[18:19]
	s_add_u32 s18, s18, 0x10000
	s_addc_u32 s19, s19, 0
	global_load_dword v120, v2, s[18:19]
	s_add_u32 s18, s18, 0x10000
	s_addc_u32 s19, s19, 0
	global_load_dword v121, v2, s[18:19]
	s_add_u32 s18, s18, 0x10000
	s_addc_u32 s19, s19, 0
	global_load_dword v122, v2, s[18:19]
	s_add_u32 s18, s18, 0x10000
	s_addc_u32 s19, s19, 0
	global_load_dword v123, v2, s[18:19]
	s_add_u32 s18, s18, 0x10000
	s_addc_u32 s19, s19, 0
	global_load_dword v124, v2, s[18:19]
	s_add_u32 s18, s18, 0x10000
	s_addc_u32 s19, s19, 0
	global_load_dword v125, v2, s[18:19]
	s_add_u32 s18, s18, 0x10000
	s_addc_u32 s19, s19, 0
	global_load_dword v126, v2, s[18:19]
	s_add_u32 s18, s18, 0x10000
	s_addc_u32 s19, s19, 0
	global_load_dword v127, v2, s[18:19]
	s_add_u32 s18, s18, 0x10000
	s_addc_u32 s19, s19, 0
	ds_read_b128 v[144:147], v20 offset:32
	ds_read_b128 v[148:151], v20 offset:48
	ds_read_b128 v[152:155], v20 offset:2080
	ds_read_b128 v[156:159], v20 offset:2096
	s_waitcnt lgkmcnt(4)
	v_bfe_u32 v21, v14, 16, 1
	v_bfe_u32 v22, v15, 16, 1
	v_add3_u32 v21, v14, v21, s11
	v_add3_u32 v22, v15, v22, s11
	v_lshrrev_b32_e32 v21, 16, v21
	v_and_or_b32 v21, v22, s12, v21
	global_store_dword v2, v21, s[20:21]
	s_add_u32 s20, s20, 0x10000
	s_addc_u32 s21, s21, 0
	s_waitcnt vmcnt(63)
	v_lshlrev_b32_e32 v23, 16, v64
	v_and_b32_e32 v24, s12, v64
	v_mul_f32_e32 v23, v136, v23
	v_mul_f32_e32 v24, v136, v24
	v_fma_f32 v14, v14, v128, v23
	v_fma_f32 v15, v15, v128, v24
	v_bfe_u32 v21, v14, 16, 1
	v_bfe_u32 v22, v15, 16, 1
	v_add3_u32 v21, v14, v21, s11
	v_add3_u32 v22, v15, v22, s11
	v_lshrrev_b32_e32 v21, 16, v21
	v_and_or_b32 v21, v22, s12, v21
	global_store_dword v2, v21, s[20:21]
	s_add_u32 s20, s20, 0x10000
	s_addc_u32 s21, s21, 0
	s_waitcnt vmcnt(63)
	v_lshlrev_b32_e32 v23, 16, v65
	v_and_b32_e32 v24, s12, v65
	v_mul_f32_e32 v23, v137, v23
	v_mul_f32_e32 v24, v137, v24
	v_fma_f32 v14, v14, v129, v23
	v_fma_f32 v15, v15, v129, v24
	v_bfe_u32 v21, v14, 16, 1
	v_bfe_u32 v22, v15, 16, 1
	v_add3_u32 v21, v14, v21, s11
	v_add3_u32 v22, v15, v22, s11
	v_lshrrev_b32_e32 v21, 16, v21
	v_and_or_b32 v21, v22, s12, v21
	global_store_dword v2, v21, s[20:21]
	s_add_u32 s20, s20, 0x10000
	s_addc_u32 s21, s21, 0
	s_waitcnt vmcnt(63)
	v_lshlrev_b32_e32 v23, 16, v66
	v_and_b32_e32 v24, s12, v66
	v_mul_f32_e32 v23, v138, v23
	v_mul_f32_e32 v24, v138, v24
	v_fma_f32 v14, v14, v130, v23
	v_fma_f32 v15, v15, v130, v24
	v_bfe_u32 v21, v14, 16, 1
	v_bfe_u32 v22, v15, 16, 1
	v_add3_u32 v21, v14, v21, s11
	v_add3_u32 v22, v15, v22, s11
	v_lshrrev_b32_e32 v21, 16, v21
	v_and_or_b32 v21, v22, s12, v21
	global_store_dword v2, v21, s[20:21]
	s_add_u32 s20, s20, 0x10000
	s_addc_u32 s21, s21, 0
	s_waitcnt vmcnt(63)
	v_lshlrev_b32_e32 v23, 16, v67
	v_and_b32_e32 v24, s12, v67
	v_mul_f32_e32 v23, v139, v23
	v_mul_f32_e32 v24, v139, v24
	v_fma_f32 v14, v14, v131, v23
	v_fma_f32 v15, v15, v131, v24
	v_bfe_u32 v21, v14, 16, 1
	v_bfe_u32 v22, v15, 16, 1
	v_add3_u32 v21, v14, v21, s11
	v_add3_u32 v22, v15, v22, s11
	v_lshrrev_b32_e32 v21, 16, v21
	v_and_or_b32 v21, v22, s12, v21
	global_store_dword v2, v21, s[20:21]
	s_add_u32 s20, s20, 0x10000
	s_addc_u32 s21, s21, 0
	s_waitcnt vmcnt(63)
	v_lshlrev_b32_e32 v23, 16, v68
	v_and_b32_e32 v24, s12, v68
	v_mul_f32_e32 v23, v140, v23
	v_mul_f32_e32 v24, v140, v24
	v_fma_f32 v14, v14, v132, v23
	v_fma_f32 v15, v15, v132, v24
	v_bfe_u32 v21, v14, 16, 1
	v_bfe_u32 v22, v15, 16, 1
	v_add3_u32 v21, v14, v21, s11
	v_add3_u32 v22, v15, v22, s11
	v_lshrrev_b32_e32 v21, 16, v21
	v_and_or_b32 v21, v22, s12, v21
	global_store_dword v2, v21, s[20:21]
	s_add_u32 s20, s20, 0x10000
	s_addc_u32 s21, s21, 0
	s_waitcnt vmcnt(63)
	v_lshlrev_b32_e32 v23, 16, v69
	v_and_b32_e32 v24, s12, v69
	v_mul_f32_e32 v23, v141, v23
	v_mul_f32_e32 v24, v141, v24
	v_fma_f32 v14, v14, v133, v23
	v_fma_f32 v15, v15, v133, v24
	v_bfe_u32 v21, v14, 16, 1
	v_bfe_u32 v22, v15, 16, 1
	v_add3_u32 v21, v14, v21, s11
	v_add3_u32 v22, v15, v22, s11
	v_lshrrev_b32_e32 v21, 16, v21
	v_and_or_b32 v21, v22, s12, v21
	global_store_dword v2, v21, s[20:21]
	s_add_u32 s20, s20, 0x10000
	s_addc_u32 s21, s21, 0
	s_waitcnt vmcnt(63)
	v_lshlrev_b32_e32 v23, 16, v70
	v_and_b32_e32 v24, s12, v70
	v_mul_f32_e32 v23, v142, v23
	v_mul_f32_e32 v24, v142, v24
	v_fma_f32 v14, v14, v134, v23
	v_fma_f32 v15, v15, v134, v24
	v_bfe_u32 v21, v14, 16, 1
	v_bfe_u32 v22, v15, 16, 1
	v_add3_u32 v21, v14, v21, s11
	v_add3_u32 v22, v15, v22, s11
	v_lshrrev_b32_e32 v21, 16, v21
	v_and_or_b32 v21, v22, s12, v21
	global_store_dword v2, v21, s[20:21]
	s_add_u32 s20, s20, 0x10000
	s_addc_u32 s21, s21, 0
	s_waitcnt vmcnt(63)
	v_lshlrev_b32_e32 v23, 16, v71
	v_and_b32_e32 v24, s12, v71
	v_mul_f32_e32 v23, v143, v23
	v_mul_f32_e32 v24, v143, v24
	v_fma_f32 v14, v14, v135, v23
	v_fma_f32 v15, v15, v135, v24
	ds_read_b128 v[128:131], v20 offset:64
	ds_read_b128 v[132:135], v20 offset:80
	ds_read_b128 v[136:139], v20 offset:2112
	ds_read_b128 v[140:143], v20 offset:2128
	s_waitcnt lgkmcnt(4)
	v_bfe_u32 v21, v14, 16, 1
	v_bfe_u32 v22, v15, 16, 1
	v_add3_u32 v21, v14, v21, s11
	v_add3_u32 v22, v15, v22, s11
	v_lshrrev_b32_e32 v21, 16, v21
	v_and_or_b32 v21, v22, s12, v21
	global_store_dword v2, v21, s[20:21]
	s_add_u32 s20, s20, 0x10000
	s_addc_u32 s21, s21, 0
	s_waitcnt vmcnt(63)
	v_lshlrev_b32_e32 v23, 16, v72
	v_and_b32_e32 v24, s12, v72
	v_mul_f32_e32 v23, v152, v23
	v_mul_f32_e32 v24, v152, v24
	v_fma_f32 v14, v14, v144, v23
	v_fma_f32 v15, v15, v144, v24
	v_bfe_u32 v21, v14, 16, 1
	v_bfe_u32 v22, v15, 16, 1
	v_add3_u32 v21, v14, v21, s11
	v_add3_u32 v22, v15, v22, s11
	v_lshrrev_b32_e32 v21, 16, v21
	v_and_or_b32 v21, v22, s12, v21
	global_store_dword v2, v21, s[20:21]
	s_add_u32 s20, s20, 0x10000
	s_addc_u32 s21, s21, 0
	s_waitcnt vmcnt(63)
	v_lshlrev_b32_e32 v23, 16, v73
	v_and_b32_e32 v24, s12, v73
	v_mul_f32_e32 v23, v153, v23
	v_mul_f32_e32 v24, v153, v24
	v_fma_f32 v14, v14, v145, v23
	v_fma_f32 v15, v15, v145, v24
	v_bfe_u32 v21, v14, 16, 1
	v_bfe_u32 v22, v15, 16, 1
	v_add3_u32 v21, v14, v21, s11
	v_add3_u32 v22, v15, v22, s11
	v_lshrrev_b32_e32 v21, 16, v21
	v_and_or_b32 v21, v22, s12, v21
	global_store_dword v2, v21, s[20:21]
	s_add_u32 s20, s20, 0x10000
	s_addc_u32 s21, s21, 0
	s_waitcnt vmcnt(63)
	v_lshlrev_b32_e32 v23, 16, v74
	v_and_b32_e32 v24, s12, v74
	v_mul_f32_e32 v23, v154, v23
	v_mul_f32_e32 v24, v154, v24
	v_fma_f32 v14, v14, v146, v23
	v_fma_f32 v15, v15, v146, v24
	v_bfe_u32 v21, v14, 16, 1
	v_bfe_u32 v22, v15, 16, 1
	v_add3_u32 v21, v14, v21, s11
	v_add3_u32 v22, v15, v22, s11
	v_lshrrev_b32_e32 v21, 16, v21
	v_and_or_b32 v21, v22, s12, v21
	global_store_dword v2, v21, s[20:21]
	s_add_u32 s20, s20, 0x10000
	s_addc_u32 s21, s21, 0
	s_waitcnt vmcnt(63)
	v_lshlrev_b32_e32 v23, 16, v75
	v_and_b32_e32 v24, s12, v75
	v_mul_f32_e32 v23, v155, v23
	v_mul_f32_e32 v24, v155, v24
	v_fma_f32 v14, v14, v147, v23
	v_fma_f32 v15, v15, v147, v24
	v_bfe_u32 v21, v14, 16, 1
	v_bfe_u32 v22, v15, 16, 1
	v_add3_u32 v21, v14, v21, s11
	v_add3_u32 v22, v15, v22, s11
	v_lshrrev_b32_e32 v21, 16, v21
	v_and_or_b32 v21, v22, s12, v21
	global_store_dword v2, v21, s[20:21]
	s_add_u32 s20, s20, 0x10000
	s_addc_u32 s21, s21, 0
	s_waitcnt vmcnt(63)
	v_lshlrev_b32_e32 v23, 16, v76
	v_and_b32_e32 v24, s12, v76
	v_mul_f32_e32 v23, v156, v23
	v_mul_f32_e32 v24, v156, v24
	v_fma_f32 v14, v14, v148, v23
	v_fma_f32 v15, v15, v148, v24
	v_bfe_u32 v21, v14, 16, 1
	v_bfe_u32 v22, v15, 16, 1
	v_add3_u32 v21, v14, v21, s11
	v_add3_u32 v22, v15, v22, s11
	v_lshrrev_b32_e32 v21, 16, v21
	v_and_or_b32 v21, v22, s12, v21
	global_store_dword v2, v21, s[20:21]
	s_add_u32 s20, s20, 0x10000
	s_addc_u32 s21, s21, 0
	s_waitcnt vmcnt(63)
	v_lshlrev_b32_e32 v23, 16, v77
	v_and_b32_e32 v24, s12, v77
	v_mul_f32_e32 v23, v157, v23
	v_mul_f32_e32 v24, v157, v24
	v_fma_f32 v14, v14, v149, v23
	v_fma_f32 v15, v15, v149, v24
	v_bfe_u32 v21, v14, 16, 1
	v_bfe_u32 v22, v15, 16, 1
	v_add3_u32 v21, v14, v21, s11
	v_add3_u32 v22, v15, v22, s11
	v_lshrrev_b32_e32 v21, 16, v21
	v_and_or_b32 v21, v22, s12, v21
	global_store_dword v2, v21, s[20:21]
	s_add_u32 s20, s20, 0x10000
	s_addc_u32 s21, s21, 0
	s_waitcnt vmcnt(63)
	v_lshlrev_b32_e32 v23, 16, v78
	v_and_b32_e32 v24, s12, v78
	v_mul_f32_e32 v23, v158, v23
	v_mul_f32_e32 v24, v158, v24
	v_fma_f32 v14, v14, v150, v23
	v_fma_f32 v15, v15, v150, v24
	v_bfe_u32 v21, v14, 16, 1
	v_bfe_u32 v22, v15, 16, 1
	v_add3_u32 v21, v14, v21, s11
	v_add3_u32 v22, v15, v22, s11
	v_lshrrev_b32_e32 v21, 16, v21
	v_and_or_b32 v21, v22, s12, v21
	global_store_dword v2, v21, s[20:21]
	s_add_u32 s20, s20, 0x10000
	s_addc_u32 s21, s21, 0
	s_waitcnt vmcnt(63)
	v_lshlrev_b32_e32 v23, 16, v79
	v_and_b32_e32 v24, s12, v79
	v_mul_f32_e32 v23, v159, v23
	v_mul_f32_e32 v24, v159, v24
	v_fma_f32 v14, v14, v151, v23
	v_fma_f32 v15, v15, v151, v24
	ds_read_b128 v[144:147], v20 offset:96
	ds_read_b128 v[148:151], v20 offset:112
	ds_read_b128 v[152:155], v20 offset:2144
	ds_read_b128 v[156:159], v20 offset:2160
	s_waitcnt lgkmcnt(4)
	v_bfe_u32 v21, v14, 16, 1
	v_bfe_u32 v22, v15, 16, 1
	v_add3_u32 v21, v14, v21, s11
	v_add3_u32 v22, v15, v22, s11
	v_lshrrev_b32_e32 v21, 16, v21
	v_and_or_b32 v21, v22, s12, v21
	global_store_dword v2, v21, s[20:21]
	s_add_u32 s20, s20, 0x10000
	s_addc_u32 s21, s21, 0
	s_waitcnt vmcnt(63)
	v_lshlrev_b32_e32 v23, 16, v80
	v_and_b32_e32 v24, s12, v80
	v_mul_f32_e32 v23, v136, v23
	v_mul_f32_e32 v24, v136, v24
	v_fma_f32 v14, v14, v128, v23
	v_fma_f32 v15, v15, v128, v24
	v_bfe_u32 v21, v14, 16, 1
	v_bfe_u32 v22, v15, 16, 1
	v_add3_u32 v21, v14, v21, s11
	v_add3_u32 v22, v15, v22, s11
	v_lshrrev_b32_e32 v21, 16, v21
	v_and_or_b32 v21, v22, s12, v21
	global_store_dword v2, v21, s[20:21]
	s_add_u32 s20, s20, 0x10000
	s_addc_u32 s21, s21, 0
	s_waitcnt vmcnt(63)
	v_lshlrev_b32_e32 v23, 16, v81
	v_and_b32_e32 v24, s12, v81
	v_mul_f32_e32 v23, v137, v23
	v_mul_f32_e32 v24, v137, v24
	v_fma_f32 v14, v14, v129, v23
	v_fma_f32 v15, v15, v129, v24
	v_bfe_u32 v21, v14, 16, 1
	v_bfe_u32 v22, v15, 16, 1
	v_add3_u32 v21, v14, v21, s11
	v_add3_u32 v22, v15, v22, s11
	v_lshrrev_b32_e32 v21, 16, v21
	v_and_or_b32 v21, v22, s12, v21
	global_store_dword v2, v21, s[20:21]
	s_add_u32 s20, s20, 0x10000
	s_addc_u32 s21, s21, 0
	s_waitcnt vmcnt(63)
	v_lshlrev_b32_e32 v23, 16, v82
	v_and_b32_e32 v24, s12, v82
	v_mul_f32_e32 v23, v138, v23
	v_mul_f32_e32 v24, v138, v24
	v_fma_f32 v14, v14, v130, v23
	v_fma_f32 v15, v15, v130, v24
	v_bfe_u32 v21, v14, 16, 1
	v_bfe_u32 v22, v15, 16, 1
	v_add3_u32 v21, v14, v21, s11
	v_add3_u32 v22, v15, v22, s11
	v_lshrrev_b32_e32 v21, 16, v21
	v_and_or_b32 v21, v22, s12, v21
	global_store_dword v2, v21, s[20:21]
	s_add_u32 s20, s20, 0x10000
	s_addc_u32 s21, s21, 0
	s_waitcnt vmcnt(63)
	v_lshlrev_b32_e32 v23, 16, v83
	v_and_b32_e32 v24, s12, v83
	v_mul_f32_e32 v23, v139, v23
	v_mul_f32_e32 v24, v139, v24
	v_fma_f32 v14, v14, v131, v23
	v_fma_f32 v15, v15, v131, v24
	v_bfe_u32 v21, v14, 16, 1
	v_bfe_u32 v22, v15, 16, 1
	v_add3_u32 v21, v14, v21, s11
	v_add3_u32 v22, v15, v22, s11
	v_lshrrev_b32_e32 v21, 16, v21
	v_and_or_b32 v21, v22, s12, v21
	global_store_dword v2, v21, s[20:21]
	s_add_u32 s20, s20, 0x10000
	s_addc_u32 s21, s21, 0
	s_waitcnt vmcnt(63)
	v_lshlrev_b32_e32 v23, 16, v84
	v_and_b32_e32 v24, s12, v84
	v_mul_f32_e32 v23, v140, v23
	v_mul_f32_e32 v24, v140, v24
	v_fma_f32 v14, v14, v132, v23
	v_fma_f32 v15, v15, v132, v24
	v_bfe_u32 v21, v14, 16, 1
	v_bfe_u32 v22, v15, 16, 1
	v_add3_u32 v21, v14, v21, s11
	v_add3_u32 v22, v15, v22, s11
	v_lshrrev_b32_e32 v21, 16, v21
	v_and_or_b32 v21, v22, s12, v21
	global_store_dword v2, v21, s[20:21]
	s_add_u32 s20, s20, 0x10000
	s_addc_u32 s21, s21, 0
	s_waitcnt vmcnt(63)
	v_lshlrev_b32_e32 v23, 16, v85
	v_and_b32_e32 v24, s12, v85
	v_mul_f32_e32 v23, v141, v23
	v_mul_f32_e32 v24, v141, v24
	v_fma_f32 v14, v14, v133, v23
	v_fma_f32 v15, v15, v133, v24
	v_bfe_u32 v21, v14, 16, 1
	v_bfe_u32 v22, v15, 16, 1
	v_add3_u32 v21, v14, v21, s11
	v_add3_u32 v22, v15, v22, s11
	v_lshrrev_b32_e32 v21, 16, v21
	v_and_or_b32 v21, v22, s12, v21
	global_store_dword v2, v21, s[20:21]
	s_add_u32 s20, s20, 0x10000
	s_addc_u32 s21, s21, 0
	s_waitcnt vmcnt(63)
	v_lshlrev_b32_e32 v23, 16, v86
	v_and_b32_e32 v24, s12, v86
	v_mul_f32_e32 v23, v142, v23
	v_mul_f32_e32 v24, v142, v24
	v_fma_f32 v14, v14, v134, v23
	v_fma_f32 v15, v15, v134, v24
	v_bfe_u32 v21, v14, 16, 1
	v_bfe_u32 v22, v15, 16, 1
	v_add3_u32 v21, v14, v21, s11
	v_add3_u32 v22, v15, v22, s11
	v_lshrrev_b32_e32 v21, 16, v21
	v_and_or_b32 v21, v22, s12, v21
	global_store_dword v2, v21, s[20:21]
	s_add_u32 s20, s20, 0x10000
	s_addc_u32 s21, s21, 0
	s_waitcnt vmcnt(63)
	v_lshlrev_b32_e32 v23, 16, v87
	v_and_b32_e32 v24, s12, v87
	v_mul_f32_e32 v23, v143, v23
	v_mul_f32_e32 v24, v143, v24
	v_fma_f32 v14, v14, v135, v23
	v_fma_f32 v15, v15, v135, v24
	ds_read_b128 v[128:131], v20 offset:128
	ds_read_b128 v[132:135], v20 offset:144
	ds_read_b128 v[136:139], v20 offset:2176
	ds_read_b128 v[140:143], v20 offset:2192
	s_waitcnt lgkmcnt(4)
	v_bfe_u32 v21, v14, 16, 1
	v_bfe_u32 v22, v15, 16, 1
	v_add3_u32 v21, v14, v21, s11
	v_add3_u32 v22, v15, v22, s11
	v_lshrrev_b32_e32 v21, 16, v21
	v_and_or_b32 v21, v22, s12, v21
	global_store_dword v2, v21, s[20:21]
	s_add_u32 s20, s20, 0x10000
	s_addc_u32 s21, s21, 0
	s_waitcnt vmcnt(63)
	v_lshlrev_b32_e32 v23, 16, v88
	v_and_b32_e32 v24, s12, v88
	v_mul_f32_e32 v23, v152, v23
	v_mul_f32_e32 v24, v152, v24
	v_fma_f32 v14, v14, v144, v23
	v_fma_f32 v15, v15, v144, v24
	v_bfe_u32 v21, v14, 16, 1
	v_bfe_u32 v22, v15, 16, 1
	v_add3_u32 v21, v14, v21, s11
	v_add3_u32 v22, v15, v22, s11
	v_lshrrev_b32_e32 v21, 16, v21
	v_and_or_b32 v21, v22, s12, v21
	global_store_dword v2, v21, s[20:21]
	s_add_u32 s20, s20, 0x10000
	s_addc_u32 s21, s21, 0
	s_waitcnt vmcnt(63)
	v_lshlrev_b32_e32 v23, 16, v89
	v_and_b32_e32 v24, s12, v89
	v_mul_f32_e32 v23, v153, v23
	v_mul_f32_e32 v24, v153, v24
	v_fma_f32 v14, v14, v145, v23
	v_fma_f32 v15, v15, v145, v24
	v_bfe_u32 v21, v14, 16, 1
	v_bfe_u32 v22, v15, 16, 1
	v_add3_u32 v21, v14, v21, s11
	v_add3_u32 v22, v15, v22, s11
	v_lshrrev_b32_e32 v21, 16, v21
	v_and_or_b32 v21, v22, s12, v21
	global_store_dword v2, v21, s[20:21]
	s_add_u32 s20, s20, 0x10000
	s_addc_u32 s21, s21, 0
	s_waitcnt vmcnt(63)
	v_lshlrev_b32_e32 v23, 16, v90
	v_and_b32_e32 v24, s12, v90
	v_mul_f32_e32 v23, v154, v23
	v_mul_f32_e32 v24, v154, v24
	v_fma_f32 v14, v14, v146, v23
	v_fma_f32 v15, v15, v146, v24
	v_bfe_u32 v21, v14, 16, 1
	v_bfe_u32 v22, v15, 16, 1
	v_add3_u32 v21, v14, v21, s11
	v_add3_u32 v22, v15, v22, s11
	v_lshrrev_b32_e32 v21, 16, v21
	v_and_or_b32 v21, v22, s12, v21
	global_store_dword v2, v21, s[20:21]
	s_add_u32 s20, s20, 0x10000
	s_addc_u32 s21, s21, 0
	s_waitcnt vmcnt(63)
	v_lshlrev_b32_e32 v23, 16, v91
	v_and_b32_e32 v24, s12, v91
	v_mul_f32_e32 v23, v155, v23
	v_mul_f32_e32 v24, v155, v24
	v_fma_f32 v14, v14, v147, v23
	v_fma_f32 v15, v15, v147, v24
	v_bfe_u32 v21, v14, 16, 1
	v_bfe_u32 v22, v15, 16, 1
	v_add3_u32 v21, v14, v21, s11
	v_add3_u32 v22, v15, v22, s11
	v_lshrrev_b32_e32 v21, 16, v21
	v_and_or_b32 v21, v22, s12, v21
	global_store_dword v2, v21, s[20:21]
	s_add_u32 s20, s20, 0x10000
	s_addc_u32 s21, s21, 0
	s_waitcnt vmcnt(63)
	v_lshlrev_b32_e32 v23, 16, v92
	v_and_b32_e32 v24, s12, v92
	v_mul_f32_e32 v23, v156, v23
	v_mul_f32_e32 v24, v156, v24
	v_fma_f32 v14, v14, v148, v23
	v_fma_f32 v15, v15, v148, v24
	v_bfe_u32 v21, v14, 16, 1
	v_bfe_u32 v22, v15, 16, 1
	v_add3_u32 v21, v14, v21, s11
	v_add3_u32 v22, v15, v22, s11
	v_lshrrev_b32_e32 v21, 16, v21
	v_and_or_b32 v21, v22, s12, v21
	global_store_dword v2, v21, s[20:21]
	s_add_u32 s20, s20, 0x10000
	s_addc_u32 s21, s21, 0
	s_waitcnt vmcnt(63)
	v_lshlrev_b32_e32 v23, 16, v93
	v_and_b32_e32 v24, s12, v93
	v_mul_f32_e32 v23, v157, v23
	v_mul_f32_e32 v24, v157, v24
	v_fma_f32 v14, v14, v149, v23
	v_fma_f32 v15, v15, v149, v24
	v_bfe_u32 v21, v14, 16, 1
	v_bfe_u32 v22, v15, 16, 1
	v_add3_u32 v21, v14, v21, s11
	v_add3_u32 v22, v15, v22, s11
	v_lshrrev_b32_e32 v21, 16, v21
	v_and_or_b32 v21, v22, s12, v21
	global_store_dword v2, v21, s[20:21]
	s_add_u32 s20, s20, 0x10000
	s_addc_u32 s21, s21, 0
	s_waitcnt vmcnt(63)
	v_lshlrev_b32_e32 v23, 16, v94
	v_and_b32_e32 v24, s12, v94
	v_mul_f32_e32 v23, v158, v23
	v_mul_f32_e32 v24, v158, v24
	v_fma_f32 v14, v14, v150, v23
	v_fma_f32 v15, v15, v150, v24
	v_bfe_u32 v21, v14, 16, 1
	v_bfe_u32 v22, v15, 16, 1
	v_add3_u32 v21, v14, v21, s11
	v_add3_u32 v22, v15, v22, s11
	v_lshrrev_b32_e32 v21, 16, v21
	v_and_or_b32 v21, v22, s12, v21
	global_store_dword v2, v21, s[20:21]
	s_add_u32 s20, s20, 0x10000
	s_addc_u32 s21, s21, 0
	s_waitcnt vmcnt(63)
	v_lshlrev_b32_e32 v23, 16, v95
	v_and_b32_e32 v24, s12, v95
	v_mul_f32_e32 v23, v159, v23
	v_mul_f32_e32 v24, v159, v24
	v_fma_f32 v14, v14, v151, v23
	v_fma_f32 v15, v15, v151, v24
	ds_read_b128 v[144:147], v20 offset:160
	ds_read_b128 v[148:151], v20 offset:176
	ds_read_b128 v[152:155], v20 offset:2208
	ds_read_b128 v[156:159], v20 offset:2224
	s_waitcnt lgkmcnt(4)
	v_bfe_u32 v21, v14, 16, 1
	v_bfe_u32 v22, v15, 16, 1
	v_add3_u32 v21, v14, v21, s11
	v_add3_u32 v22, v15, v22, s11
	v_lshrrev_b32_e32 v21, 16, v21
	v_and_or_b32 v21, v22, s12, v21
	global_store_dword v2, v21, s[20:21]
	s_add_u32 s20, s20, 0x10000
	s_addc_u32 s21, s21, 0
	s_waitcnt vmcnt(63)
	v_lshlrev_b32_e32 v23, 16, v96
	v_and_b32_e32 v24, s12, v96
	v_mul_f32_e32 v23, v136, v23
	v_mul_f32_e32 v24, v136, v24
	v_fma_f32 v14, v14, v128, v23
	v_fma_f32 v15, v15, v128, v24
	v_bfe_u32 v21, v14, 16, 1
	v_bfe_u32 v22, v15, 16, 1
	v_add3_u32 v21, v14, v21, s11
	v_add3_u32 v22, v15, v22, s11
	v_lshrrev_b32_e32 v21, 16, v21
	v_and_or_b32 v21, v22, s12, v21
	global_store_dword v2, v21, s[20:21]
	s_add_u32 s20, s20, 0x10000
	s_addc_u32 s21, s21, 0
	s_waitcnt vmcnt(63)
	v_lshlrev_b32_e32 v23, 16, v97
	v_and_b32_e32 v24, s12, v97
	v_mul_f32_e32 v23, v137, v23
	v_mul_f32_e32 v24, v137, v24
	v_fma_f32 v14, v14, v129, v23
	v_fma_f32 v15, v15, v129, v24
	v_bfe_u32 v21, v14, 16, 1
	v_bfe_u32 v22, v15, 16, 1
	v_add3_u32 v21, v14, v21, s11
	v_add3_u32 v22, v15, v22, s11
	v_lshrrev_b32_e32 v21, 16, v21
	v_and_or_b32 v21, v22, s12, v21
	global_store_dword v2, v21, s[20:21]
	s_add_u32 s20, s20, 0x10000
	s_addc_u32 s21, s21, 0
	s_waitcnt vmcnt(63)
	v_lshlrev_b32_e32 v23, 16, v98
	v_and_b32_e32 v24, s12, v98
	v_mul_f32_e32 v23, v138, v23
	v_mul_f32_e32 v24, v138, v24
	v_fma_f32 v14, v14, v130, v23
	v_fma_f32 v15, v15, v130, v24
	v_bfe_u32 v21, v14, 16, 1
	v_bfe_u32 v22, v15, 16, 1
	v_add3_u32 v21, v14, v21, s11
	v_add3_u32 v22, v15, v22, s11
	v_lshrrev_b32_e32 v21, 16, v21
	v_and_or_b32 v21, v22, s12, v21
	global_store_dword v2, v21, s[20:21]
	s_add_u32 s20, s20, 0x10000
	s_addc_u32 s21, s21, 0
	s_waitcnt vmcnt(63)
	v_lshlrev_b32_e32 v23, 16, v99
	v_and_b32_e32 v24, s12, v99
	v_mul_f32_e32 v23, v139, v23
	v_mul_f32_e32 v24, v139, v24
	v_fma_f32 v14, v14, v131, v23
	v_fma_f32 v15, v15, v131, v24
	v_bfe_u32 v21, v14, 16, 1
	v_bfe_u32 v22, v15, 16, 1
	v_add3_u32 v21, v14, v21, s11
	v_add3_u32 v22, v15, v22, s11
	v_lshrrev_b32_e32 v21, 16, v21
	v_and_or_b32 v21, v22, s12, v21
	global_store_dword v2, v21, s[20:21]
	s_add_u32 s20, s20, 0x10000
	s_addc_u32 s21, s21, 0
	s_waitcnt vmcnt(63)
	v_lshlrev_b32_e32 v23, 16, v100
	v_and_b32_e32 v24, s12, v100
	v_mul_f32_e32 v23, v140, v23
	v_mul_f32_e32 v24, v140, v24
	v_fma_f32 v14, v14, v132, v23
	v_fma_f32 v15, v15, v132, v24
	v_bfe_u32 v21, v14, 16, 1
	v_bfe_u32 v22, v15, 16, 1
	v_add3_u32 v21, v14, v21, s11
	v_add3_u32 v22, v15, v22, s11
	v_lshrrev_b32_e32 v21, 16, v21
	v_and_or_b32 v21, v22, s12, v21
	global_store_dword v2, v21, s[20:21]
	s_add_u32 s20, s20, 0x10000
	s_addc_u32 s21, s21, 0
	s_waitcnt vmcnt(63)
	v_lshlrev_b32_e32 v23, 16, v101
	v_and_b32_e32 v24, s12, v101
	v_mul_f32_e32 v23, v141, v23
	v_mul_f32_e32 v24, v141, v24
	v_fma_f32 v14, v14, v133, v23
	v_fma_f32 v15, v15, v133, v24
	v_bfe_u32 v21, v14, 16, 1
	v_bfe_u32 v22, v15, 16, 1
	v_add3_u32 v21, v14, v21, s11
	v_add3_u32 v22, v15, v22, s11
	v_lshrrev_b32_e32 v21, 16, v21
	v_and_or_b32 v21, v22, s12, v21
	global_store_dword v2, v21, s[20:21]
	s_add_u32 s20, s20, 0x10000
	s_addc_u32 s21, s21, 0
	s_waitcnt vmcnt(63)
	v_lshlrev_b32_e32 v23, 16, v102
	v_and_b32_e32 v24, s12, v102
	v_mul_f32_e32 v23, v142, v23
	v_mul_f32_e32 v24, v142, v24
	v_fma_f32 v14, v14, v134, v23
	v_fma_f32 v15, v15, v134, v24
	v_bfe_u32 v21, v14, 16, 1
	v_bfe_u32 v22, v15, 16, 1
	v_add3_u32 v21, v14, v21, s11
	v_add3_u32 v22, v15, v22, s11
	v_lshrrev_b32_e32 v21, 16, v21
	v_and_or_b32 v21, v22, s12, v21
	global_store_dword v2, v21, s[20:21]
	s_add_u32 s20, s20, 0x10000
	s_addc_u32 s21, s21, 0
	s_waitcnt vmcnt(63)
	v_lshlrev_b32_e32 v23, 16, v103
	v_and_b32_e32 v24, s12, v103
	v_mul_f32_e32 v23, v143, v23
	v_mul_f32_e32 v24, v143, v24
	v_fma_f32 v14, v14, v135, v23
	v_fma_f32 v15, v15, v135, v24
	ds_read_b128 v[128:131], v20 offset:192
	ds_read_b128 v[132:135], v20 offset:208
	ds_read_b128 v[136:139], v20 offset:2240
	ds_read_b128 v[140:143], v20 offset:2256
	s_waitcnt lgkmcnt(4)
	v_bfe_u32 v21, v14, 16, 1
	v_bfe_u32 v22, v15, 16, 1
	v_add3_u32 v21, v14, v21, s11
	v_add3_u32 v22, v15, v22, s11
	v_lshrrev_b32_e32 v21, 16, v21
	v_and_or_b32 v21, v22, s12, v21
	global_store_dword v2, v21, s[20:21]
	s_add_u32 s20, s20, 0x10000
	s_addc_u32 s21, s21, 0
	s_waitcnt vmcnt(63)
	v_lshlrev_b32_e32 v23, 16, v104
	v_and_b32_e32 v24, s12, v104
	v_mul_f32_e32 v23, v152, v23
	v_mul_f32_e32 v24, v152, v24
	v_fma_f32 v14, v14, v144, v23
	v_fma_f32 v15, v15, v144, v24
	v_bfe_u32 v21, v14, 16, 1
	v_bfe_u32 v22, v15, 16, 1
	v_add3_u32 v21, v14, v21, s11
	v_add3_u32 v22, v15, v22, s11
	v_lshrrev_b32_e32 v21, 16, v21
	v_and_or_b32 v21, v22, s12, v21
	global_store_dword v2, v21, s[20:21]
	s_add_u32 s20, s20, 0x10000
	s_addc_u32 s21, s21, 0
	s_waitcnt vmcnt(63)
	v_lshlrev_b32_e32 v23, 16, v105
	v_and_b32_e32 v24, s12, v105
	v_mul_f32_e32 v23, v153, v23
	v_mul_f32_e32 v24, v153, v24
	v_fma_f32 v14, v14, v145, v23
	v_fma_f32 v15, v15, v145, v24
	v_bfe_u32 v21, v14, 16, 1
	v_bfe_u32 v22, v15, 16, 1
	v_add3_u32 v21, v14, v21, s11
	v_add3_u32 v22, v15, v22, s11
	v_lshrrev_b32_e32 v21, 16, v21
	v_and_or_b32 v21, v22, s12, v21
	global_store_dword v2, v21, s[20:21]
	s_add_u32 s20, s20, 0x10000
	s_addc_u32 s21, s21, 0
	s_waitcnt vmcnt(63)
	v_lshlrev_b32_e32 v23, 16, v106
	v_and_b32_e32 v24, s12, v106
	v_mul_f32_e32 v23, v154, v23
	v_mul_f32_e32 v24, v154, v24
	v_fma_f32 v14, v14, v146, v23
	v_fma_f32 v15, v15, v146, v24
	v_bfe_u32 v21, v14, 16, 1
	v_bfe_u32 v22, v15, 16, 1
	v_add3_u32 v21, v14, v21, s11
	v_add3_u32 v22, v15, v22, s11
	v_lshrrev_b32_e32 v21, 16, v21
	v_and_or_b32 v21, v22, s12, v21
	global_store_dword v2, v21, s[20:21]
	s_add_u32 s20, s20, 0x10000
	s_addc_u32 s21, s21, 0
	s_waitcnt vmcnt(63)
	v_lshlrev_b32_e32 v23, 16, v107
	v_and_b32_e32 v24, s12, v107
	v_mul_f32_e32 v23, v155, v23
	v_mul_f32_e32 v24, v155, v24
	v_fma_f32 v14, v14, v147, v23
	v_fma_f32 v15, v15, v147, v24
	v_bfe_u32 v21, v14, 16, 1
	v_bfe_u32 v22, v15, 16, 1
	v_add3_u32 v21, v14, v21, s11
	v_add3_u32 v22, v15, v22, s11
	v_lshrrev_b32_e32 v21, 16, v21
	v_and_or_b32 v21, v22, s12, v21
	global_store_dword v2, v21, s[20:21]
	s_add_u32 s20, s20, 0x10000
	s_addc_u32 s21, s21, 0
	s_waitcnt vmcnt(63)
	v_lshlrev_b32_e32 v23, 16, v108
	v_and_b32_e32 v24, s12, v108
	v_mul_f32_e32 v23, v156, v23
	v_mul_f32_e32 v24, v156, v24
	v_fma_f32 v14, v14, v148, v23
	v_fma_f32 v15, v15, v148, v24
	v_bfe_u32 v21, v14, 16, 1
	v_bfe_u32 v22, v15, 16, 1
	v_add3_u32 v21, v14, v21, s11
	v_add3_u32 v22, v15, v22, s11
	v_lshrrev_b32_e32 v21, 16, v21
	v_and_or_b32 v21, v22, s12, v21
	global_store_dword v2, v21, s[20:21]
	s_add_u32 s20, s20, 0x10000
	s_addc_u32 s21, s21, 0
	s_waitcnt vmcnt(63)
	v_lshlrev_b32_e32 v23, 16, v109
	v_and_b32_e32 v24, s12, v109
	v_mul_f32_e32 v23, v157, v23
	v_mul_f32_e32 v24, v157, v24
	v_fma_f32 v14, v14, v149, v23
	v_fma_f32 v15, v15, v149, v24
	v_bfe_u32 v21, v14, 16, 1
	v_bfe_u32 v22, v15, 16, 1
	v_add3_u32 v21, v14, v21, s11
	v_add3_u32 v22, v15, v22, s11
	v_lshrrev_b32_e32 v21, 16, v21
	v_and_or_b32 v21, v22, s12, v21
	global_store_dword v2, v21, s[20:21]
	s_add_u32 s20, s20, 0x10000
	s_addc_u32 s21, s21, 0
	s_waitcnt vmcnt(63)
	v_lshlrev_b32_e32 v23, 16, v110
	v_and_b32_e32 v24, s12, v110
	v_mul_f32_e32 v23, v158, v23
	v_mul_f32_e32 v24, v158, v24
	v_fma_f32 v14, v14, v150, v23
	v_fma_f32 v15, v15, v150, v24
	v_bfe_u32 v21, v14, 16, 1
	v_bfe_u32 v22, v15, 16, 1
	v_add3_u32 v21, v14, v21, s11
	v_add3_u32 v22, v15, v22, s11
	v_lshrrev_b32_e32 v21, 16, v21
	v_and_or_b32 v21, v22, s12, v21
	global_store_dword v2, v21, s[20:21]
	s_add_u32 s20, s20, 0x10000
	s_addc_u32 s21, s21, 0
	s_waitcnt vmcnt(63)
	v_lshlrev_b32_e32 v23, 16, v111
	v_and_b32_e32 v24, s12, v111
	v_mul_f32_e32 v23, v159, v23
	v_mul_f32_e32 v24, v159, v24
	v_fma_f32 v14, v14, v151, v23
	v_fma_f32 v15, v15, v151, v24
	ds_read_b128 v[144:147], v20 offset:224
	ds_read_b128 v[148:151], v20 offset:240
	ds_read_b128 v[152:155], v20 offset:2272
	ds_read_b128 v[156:159], v20 offset:2288
	s_waitcnt lgkmcnt(4)
	v_bfe_u32 v21, v14, 16, 1
	v_bfe_u32 v22, v15, 16, 1
	v_add3_u32 v21, v14, v21, s11
	v_add3_u32 v22, v15, v22, s11
	v_lshrrev_b32_e32 v21, 16, v21
	v_and_or_b32 v21, v22, s12, v21
	global_store_dword v2, v21, s[20:21]
	s_add_u32 s20, s20, 0x10000
	s_addc_u32 s21, s21, 0
	s_waitcnt vmcnt(63)
	v_lshlrev_b32_e32 v23, 16, v112
	v_and_b32_e32 v24, s12, v112
	v_mul_f32_e32 v23, v136, v23
	v_mul_f32_e32 v24, v136, v24
	v_fma_f32 v14, v14, v128, v23
	v_fma_f32 v15, v15, v128, v24
	v_bfe_u32 v21, v14, 16, 1
	v_bfe_u32 v22, v15, 16, 1
	v_add3_u32 v21, v14, v21, s11
	v_add3_u32 v22, v15, v22, s11
	v_lshrrev_b32_e32 v21, 16, v21
	v_and_or_b32 v21, v22, s12, v21
	global_store_dword v2, v21, s[20:21]
	s_add_u32 s20, s20, 0x10000
	s_addc_u32 s21, s21, 0
	s_waitcnt vmcnt(63)
	v_lshlrev_b32_e32 v23, 16, v113
	v_and_b32_e32 v24, s12, v113
	v_mul_f32_e32 v23, v137, v23
	v_mul_f32_e32 v24, v137, v24
	v_fma_f32 v14, v14, v129, v23
	v_fma_f32 v15, v15, v129, v24
	v_bfe_u32 v21, v14, 16, 1
	v_bfe_u32 v22, v15, 16, 1
	v_add3_u32 v21, v14, v21, s11
	v_add3_u32 v22, v15, v22, s11
	v_lshrrev_b32_e32 v21, 16, v21
	v_and_or_b32 v21, v22, s12, v21
	global_store_dword v2, v21, s[20:21]
	s_add_u32 s20, s20, 0x10000
	s_addc_u32 s21, s21, 0
	s_waitcnt vmcnt(63)
	v_lshlrev_b32_e32 v23, 16, v114
	v_and_b32_e32 v24, s12, v114
	v_mul_f32_e32 v23, v138, v23
	v_mul_f32_e32 v24, v138, v24
	v_fma_f32 v14, v14, v130, v23
	v_fma_f32 v15, v15, v130, v24
	v_bfe_u32 v21, v14, 16, 1
	v_bfe_u32 v22, v15, 16, 1
	v_add3_u32 v21, v14, v21, s11
	v_add3_u32 v22, v15, v22, s11
	v_lshrrev_b32_e32 v21, 16, v21
	v_and_or_b32 v21, v22, s12, v21
	global_store_dword v2, v21, s[20:21]
	s_add_u32 s20, s20, 0x10000
	s_addc_u32 s21, s21, 0
	s_waitcnt vmcnt(63)
	v_lshlrev_b32_e32 v23, 16, v115
	v_and_b32_e32 v24, s12, v115
	v_mul_f32_e32 v23, v139, v23
	v_mul_f32_e32 v24, v139, v24
	v_fma_f32 v14, v14, v131, v23
	v_fma_f32 v15, v15, v131, v24
	v_bfe_u32 v21, v14, 16, 1
	v_bfe_u32 v22, v15, 16, 1
	v_add3_u32 v21, v14, v21, s11
	v_add3_u32 v22, v15, v22, s11
	v_lshrrev_b32_e32 v21, 16, v21
	v_and_or_b32 v21, v22, s12, v21
	global_store_dword v2, v21, s[20:21]
	s_add_u32 s20, s20, 0x10000
	s_addc_u32 s21, s21, 0
	s_waitcnt vmcnt(63)
	v_lshlrev_b32_e32 v23, 16, v116
	v_and_b32_e32 v24, s12, v116
	v_mul_f32_e32 v23, v140, v23
	v_mul_f32_e32 v24, v140, v24
	v_fma_f32 v14, v14, v132, v23
	v_fma_f32 v15, v15, v132, v24
	v_bfe_u32 v21, v14, 16, 1
	v_bfe_u32 v22, v15, 16, 1
	v_add3_u32 v21, v14, v21, s11
	v_add3_u32 v22, v15, v22, s11
	v_lshrrev_b32_e32 v21, 16, v21
	v_and_or_b32 v21, v22, s12, v21
	global_store_dword v2, v21, s[20:21]
	s_add_u32 s20, s20, 0x10000
	s_addc_u32 s21, s21, 0
	s_waitcnt vmcnt(63)
	v_lshlrev_b32_e32 v23, 16, v117
	v_and_b32_e32 v24, s12, v117
	v_mul_f32_e32 v23, v141, v23
	v_mul_f32_e32 v24, v141, v24
	v_fma_f32 v14, v14, v133, v23
	v_fma_f32 v15, v15, v133, v24
	v_bfe_u32 v21, v14, 16, 1
	v_bfe_u32 v22, v15, 16, 1
	v_add3_u32 v21, v14, v21, s11
	v_add3_u32 v22, v15, v22, s11
	v_lshrrev_b32_e32 v21, 16, v21
	v_and_or_b32 v21, v22, s12, v21
	global_store_dword v2, v21, s[20:21]
	s_add_u32 s20, s20, 0x10000
	s_addc_u32 s21, s21, 0
	s_waitcnt vmcnt(63)
	v_lshlrev_b32_e32 v23, 16, v118
	v_and_b32_e32 v24, s12, v118
	v_mul_f32_e32 v23, v142, v23
	v_mul_f32_e32 v24, v142, v24
	v_fma_f32 v14, v14, v134, v23
	v_fma_f32 v15, v15, v134, v24
	v_bfe_u32 v21, v14, 16, 1
	v_bfe_u32 v22, v15, 16, 1
	v_add3_u32 v21, v14, v21, s11
	v_add3_u32 v22, v15, v22, s11
	v_lshrrev_b32_e32 v21, 16, v21
	v_and_or_b32 v21, v22, s12, v21
	global_store_dword v2, v21, s[20:21]
	s_add_u32 s20, s20, 0x10000
	s_addc_u32 s21, s21, 0
	s_waitcnt vmcnt(63)
	v_lshlrev_b32_e32 v23, 16, v119
	v_and_b32_e32 v24, s12, v119
	v_mul_f32_e32 v23, v143, v23
	v_mul_f32_e32 v24, v143, v24
	v_fma_f32 v14, v14, v135, v23
	v_fma_f32 v15, v15, v135, v24
	s_waitcnt lgkmcnt(0)
	v_bfe_u32 v21, v14, 16, 1
	v_bfe_u32 v22, v15, 16, 1
	v_add3_u32 v21, v14, v21, s11
	v_add3_u32 v22, v15, v22, s11
	v_lshrrev_b32_e32 v21, 16, v21
	v_and_or_b32 v21, v22, s12, v21
	global_store_dword v2, v21, s[20:21]
	s_add_u32 s20, s20, 0x10000
	s_addc_u32 s21, s21, 0
	s_waitcnt vmcnt(63)
	v_lshlrev_b32_e32 v23, 16, v120
	v_and_b32_e32 v24, s12, v120
	v_mul_f32_e32 v23, v152, v23
	v_mul_f32_e32 v24, v152, v24
	v_fma_f32 v14, v14, v144, v23
	v_fma_f32 v15, v15, v144, v24
	v_bfe_u32 v21, v14, 16, 1
	v_bfe_u32 v22, v15, 16, 1
	v_add3_u32 v21, v14, v21, s11
	v_add3_u32 v22, v15, v22, s11
	v_lshrrev_b32_e32 v21, 16, v21
	v_and_or_b32 v21, v22, s12, v21
	global_store_dword v2, v21, s[20:21]
	s_add_u32 s20, s20, 0x10000
	s_addc_u32 s21, s21, 0
	s_waitcnt vmcnt(63)
	v_lshlrev_b32_e32 v23, 16, v121
	v_and_b32_e32 v24, s12, v121
	v_mul_f32_e32 v23, v153, v23
	v_mul_f32_e32 v24, v153, v24
	v_fma_f32 v14, v14, v145, v23
	v_fma_f32 v15, v15, v145, v24
	v_bfe_u32 v21, v14, 16, 1
	v_bfe_u32 v22, v15, 16, 1
	v_add3_u32 v21, v14, v21, s11
	v_add3_u32 v22, v15, v22, s11
	v_lshrrev_b32_e32 v21, 16, v21
	v_and_or_b32 v21, v22, s12, v21
	global_store_dword v2, v21, s[20:21]
	s_add_u32 s20, s20, 0x10000
	s_addc_u32 s21, s21, 0
	s_waitcnt vmcnt(63)
	v_lshlrev_b32_e32 v23, 16, v122
	v_and_b32_e32 v24, s12, v122
	v_mul_f32_e32 v23, v154, v23
	v_mul_f32_e32 v24, v154, v24
	v_fma_f32 v14, v14, v146, v23
	v_fma_f32 v15, v15, v146, v24
	v_bfe_u32 v21, v14, 16, 1
	v_bfe_u32 v22, v15, 16, 1
	v_add3_u32 v21, v14, v21, s11
	v_add3_u32 v22, v15, v22, s11
	v_lshrrev_b32_e32 v21, 16, v21
	v_and_or_b32 v21, v22, s12, v21
	global_store_dword v2, v21, s[20:21]
	s_add_u32 s20, s20, 0x10000
	s_addc_u32 s21, s21, 0
	s_waitcnt vmcnt(63)
	v_lshlrev_b32_e32 v23, 16, v123
	v_and_b32_e32 v24, s12, v123
	v_mul_f32_e32 v23, v155, v23
	v_mul_f32_e32 v24, v155, v24
	v_fma_f32 v14, v14, v147, v23
	v_fma_f32 v15, v15, v147, v24
	v_bfe_u32 v21, v14, 16, 1
	v_bfe_u32 v22, v15, 16, 1
	v_add3_u32 v21, v14, v21, s11
	v_add3_u32 v22, v15, v22, s11
	v_lshrrev_b32_e32 v21, 16, v21
	v_and_or_b32 v21, v22, s12, v21
	global_store_dword v2, v21, s[20:21]
	s_add_u32 s20, s20, 0x10000
	s_addc_u32 s21, s21, 0
	s_waitcnt vmcnt(63)
	v_lshlrev_b32_e32 v23, 16, v124
	v_and_b32_e32 v24, s12, v124
	v_mul_f32_e32 v23, v156, v23
	v_mul_f32_e32 v24, v156, v24
	v_fma_f32 v14, v14, v148, v23
	v_fma_f32 v15, v15, v148, v24
	v_bfe_u32 v21, v14, 16, 1
	v_bfe_u32 v22, v15, 16, 1
	v_add3_u32 v21, v14, v21, s11
	v_add3_u32 v22, v15, v22, s11
	v_lshrrev_b32_e32 v21, 16, v21
	v_and_or_b32 v21, v22, s12, v21
	global_store_dword v2, v21, s[20:21]
	s_add_u32 s20, s20, 0x10000
	s_addc_u32 s21, s21, 0
	s_waitcnt vmcnt(63)
	v_lshlrev_b32_e32 v23, 16, v125
	v_and_b32_e32 v24, s12, v125
	v_mul_f32_e32 v23, v157, v23
	v_mul_f32_e32 v24, v157, v24
	v_fma_f32 v14, v14, v149, v23
	v_fma_f32 v15, v15, v149, v24
	v_bfe_u32 v21, v14, 16, 1
	v_bfe_u32 v22, v15, 16, 1
	v_add3_u32 v21, v14, v21, s11
	v_add3_u32 v22, v15, v22, s11
	v_lshrrev_b32_e32 v21, 16, v21
	v_and_or_b32 v21, v22, s12, v21
	global_store_dword v2, v21, s[20:21]
	s_add_u32 s20, s20, 0x10000
	s_addc_u32 s21, s21, 0
	s_waitcnt vmcnt(63)
	v_lshlrev_b32_e32 v23, 16, v126
	v_and_b32_e32 v24, s12, v126
	v_mul_f32_e32 v23, v158, v23
	v_mul_f32_e32 v24, v158, v24
	v_fma_f32 v14, v14, v150, v23
	v_fma_f32 v15, v15, v150, v24
	v_bfe_u32 v21, v14, 16, 1
	v_bfe_u32 v22, v15, 16, 1
	v_add3_u32 v21, v14, v21, s11
	v_add3_u32 v22, v15, v22, s11
	v_lshrrev_b32_e32 v21, 16, v21
	v_and_or_b32 v21, v22, s12, v21
	global_store_dword v2, v21, s[20:21]
	s_add_u32 s20, s20, 0x10000
	s_addc_u32 s21, s21, 0
	s_waitcnt vmcnt(63)
	v_lshlrev_b32_e32 v23, 16, v127
	v_and_b32_e32 v24, s12, v127
	v_mul_f32_e32 v23, v159, v23
	v_mul_f32_e32 v24, v159, v24
	v_fma_f32 v14, v14, v151, v23
	v_fma_f32 v15, v15, v151, v24
	v_add_u32_e32 v19, s8, v19
	v_cmp_lt_i32_e32 vcc, s27, v19
	s_or_b64 s[2:3], vcc, s[2:3]
	v_add_u32_e32 v18, s9, v18
	s_andn2_b64 exec, exec, s[2:3]
	s_cbranch_execnz .LBB0_694
